# v44
# speedup vs baseline: 1.0052x; 1.0052x over previous
_Z3k_BPKiS0_PiS1_PKfPDF16_:
	v_cmp_eq_u32_e32 vcc, 0, v0
	s_and_saveexec_b64 s[4:5], vcc
	v_mov_b32_e32 v2, 0
	v_mov_b32_e32 v3, v2
	ds_write_b64 v2, v[2:3] offset:27712
	s_or_b64 exec, exec, s[4:5]
	s_load_dwordx2 s[24:25], s[0:1], 0x0
	s_load_dwordx4 s[36:39], s[0:1], 0x20
	s_movk_i32 s3, 0x100
	v_cmp_gt_u32_e32 vcc, s3, v0
	v_mbcnt_lo_u32_b32 v16, -1, 0
	v_and_b32_e32 v14, 63, v0
	s_waitcnt lgkmcnt(0)
	s_barrier
	s_lshl_b32 s40, s2, 10
	s_add_i32 s40, s40, 0x124f80
	v_add_u32_e32 v60, s40, v0
	v_min_u32_e32 v61, 0x1869ff, v60
	v_lshlrev_b32_e32 v61, 5, v61
	global_load_dwordx4 v[28:31], v61, s[36:37]
	global_load_dwordx4 v[32:35], v61, s[36:37] offset:16
	s_and_saveexec_b64 s[6:7], vcc
	s_cbranch_execz .LBB1_12
	s_setprio 2
	s_load_dwordx2 s[4:5], s[0:1], 0x8
	s_lshl_b32 s3, s2, 8
	v_or_b32_e32 v2, s3, v0
	s_addk_i32 s3, 0x100
	v_ashrrev_i32_e32 v3, 31, v2
	v_or_b32_e32 v4, s3, v0
	s_waitcnt lgkmcnt(0)
	v_lshl_add_u64 v[2:3], v[2:3], 2, s[4:5]
	v_ashrrev_i32_e32 v5, 31, v4
	v_lshl_add_u64 v[4:5], v[4:5], 2, s[4:5]
	global_load_dword v1, v[2:3], off
	global_load_dword v6, v[4:5], off
	v_mbcnt_hi_u32_b32 v2, -1, v16
	v_and_b32_e32 v3, 64, v2
	v_xor_b32_e32 v4, 32, v2
	v_add_u32_e32 v3, 64, v3
	v_cmp_lt_i32_e64 s[4:5], v4, v3
	v_xor_b32_e32 v7, 16, v2
	v_xor_b32_e32 v8, 8, v2
	v_cndmask_b32_e64 v4, v2, v4, s[4:5]
	v_lshlrev_b32_e32 v4, 2, v4
	v_cmp_lt_i32_e64 s[4:5], v7, v3
	v_xor_b32_e32 v9, 4, v2
	v_xor_b32_e32 v10, 2, v2
	v_cndmask_b32_e64 v7, v2, v7, s[4:5]
	v_lshlrev_b32_e32 v7, 2, v7
	v_cmp_lt_i32_e64 s[4:5], v8, v3
	v_xor_b32_e32 v11, 1, v2
	s_movk_i32 s3, 0x1870
	v_cndmask_b32_e64 v8, v2, v8, s[4:5]
	v_lshlrev_b32_e32 v8, 2, v8
	v_cmp_lt_i32_e64 s[4:5], v9, v3
	v_lshlrev_b32_e32 v5, 2, v0
	s_waitcnt vmcnt(1)
	ds_bpermute_b32 v12, v4, v1
	s_waitcnt vmcnt(0)
	v_sub_u32_e32 v6, v6, v1
	ds_bpermute_b32 v4, v4, v6
	v_cndmask_b32_e64 v9, v2, v9, s[4:5]
	v_lshlrev_b32_e32 v9, 2, v9
	s_waitcnt lgkmcnt(1)
	v_add_u32_e32 v12, v12, v1
	ds_bpermute_b32 v13, v7, v12
	s_waitcnt lgkmcnt(1)
	v_add_u32_e32 v4, v4, v6
	ds_bpermute_b32 v7, v7, v4
	v_cmp_lt_i32_e64 s[4:5], v10, v3
	s_waitcnt lgkmcnt(1)
	v_add_u32_e32 v12, v13, v12
	v_cndmask_b32_e64 v10, v2, v10, s[4:5]
	s_waitcnt lgkmcnt(0)
	v_add_u32_e32 v4, v7, v4
	ds_bpermute_b32 v7, v8, v12
	ds_bpermute_b32 v8, v8, v4
	v_lshlrev_b32_e32 v10, 2, v10
	v_cmp_lt_i32_e64 s[4:5], v11, v3
	s_waitcnt lgkmcnt(1)
	v_add_u32_e32 v7, v7, v12
	s_waitcnt lgkmcnt(0)
	v_add_u32_e32 v4, v8, v4
	ds_bpermute_b32 v8, v9, v7
	ds_bpermute_b32 v9, v9, v4
	v_cndmask_b32_e64 v2, v2, v11, s[4:5]
	v_lshlrev_b32_e32 v2, 2, v2
	v_cmp_eq_u32_e64 s[4:5], 0, v14
	s_waitcnt lgkmcnt(1)
	v_add_u32_e32 v7, v8, v7
	s_waitcnt lgkmcnt(0)
	v_add_u32_e32 v4, v9, v4
	ds_bpermute_b32 v8, v10, v7
	ds_bpermute_b32 v9, v10, v4
	v_mad_u32_u24 v10, v0, s3, v1
	ds_write2st64_b32 v5, v6, v10 offset0:96 offset1:100
	v_mov_b32_e32 v6, 0
	s_waitcnt lgkmcnt(2)
	v_add_u32_e32 v3, v8, v7
	s_waitcnt lgkmcnt(1)
	v_add_u32_e32 v1, v9, v4
	ds_bpermute_b32 v4, v2, v3
	ds_bpermute_b32 v2, v2, v1
	ds_write_b32 v5, v6 offset:26624
	s_and_b64 exec, exec, s[4:5]
	s_cbranch_execz .LBB1_12
	s_mov_b64 s[4:5], exec
	s_waitcnt lgkmcnt(2)
	v_add_u32_e32 v3, v4, v3
	s_mov_b32 s8, 0

.LBB1_12:
	s_setprio 0
	s_or_b64 exec, exec, s[6:7]
	v_lshrrev_b32_e32 v1, 5, v0
	s_waitcnt lgkmcnt(2)
	v_lshlrev_b32_e32 v4, 2, v1
	s_waitcnt lgkmcnt(0)
	s_barrier
	s_waitcnt vmcnt(0)
	ds_read_b32 v24, v4 offset:24576
	v_and_b32_e32 v1, 31, v0
	v_or_b32_e32 v5, 0x6000, v4
	v_mov_b32_e32 v13, -1
	v_mov_b32_e32 v15, -1
	s_waitcnt lgkmcnt(0)
	v_cmp_lt_i32_e64 s[4:5], v1, v24
	s_and_saveexec_b64 s[6:7], s[4:5]
	s_cbranch_execz .LBB1_14
	ds_read_b32 v2, v4 offset:25600
	s_waitcnt lgkmcnt(0)
	v_add_u32_e32 v2, v2, v1
	v_ashrrev_i32_e32 v3, 31, v2
	v_lshl_add_u64 v[2:3], v[2:3], 2, s[24:25]
	global_load_dword v15, v[2:3], off
